# speedup vs baseline: 1.0106x; 1.0106x over previous
.LBB3_1:
	s_waitcnt vmcnt(4)
	s_lshl_b32 s18, s23, 14
	s_barrier
	v_or_b32_e32 v144, s18, v115
	v_add_u32_e32 v154, v144, v116
	v_add_u32_e32 v155, v144, v117
	v_add_u32_e32 v156, v144, v118
	v_add_u32_e32 v157, v144, v119
	ds_read_b128 v[50:53], v154
	ds_read_b128 v[120:123], v154 offset:4096
	ds_read_b128 v[124:127], v155
	ds_read_b128 v[128:131], v155 offset:4096
	ds_read_b128 v[132:135], v156
	ds_read_b128 v[136:139], v156 offset:4096
	ds_read_b128 v[140:143], v157
	ds_read_b128 v[150:153], v157 offset:4096
	s_add_i32 s6, s18, 0xffffc000
	s_cmp_lg_u32 s23, 0
	s_cselect_b32 s6, s6, 0x8000
	s_add_i32 s6, s22, s6
	s_waitcnt lgkmcnt(4)
	s_setprio 1
	v_mfma_f32_32x32x16_f16 v[66:81], v[50:53], v[94:97], v[34:49]
	s_mov_b32 m0, s6
	s_add_i32 s7, s6, 0x400
	v_mfma_f32_32x32x16_f16 v[50:65], v[120:123], v[94:97], v[34:49]
	global_load_lds_dwordx4 v145, s[36:37]
	s_mov_b32 m0, s7
	v_mfma_f32_32x32x16_f16 v[66:81], v[124:127], v[90:93], v[66:81]
	s_add_i32 s7, s6, 0x2000
	global_load_lds_dwordx4 v149, s[36:37]
	v_mfma_f32_32x32x16_f16 v[50:65], v[128:131], v[90:93], v[50:65]
	s_mov_b32 m0, s7
	s_add_i32 s7, s6, 0x2400
	s_waitcnt lgkmcnt(0)
	v_mfma_f32_32x32x16_f16 v[66:81], v[132:135], v[86:89], v[66:81]
	global_load_lds_dwordx4 v148, s[38:39]
	v_mfma_f32_32x32x16_f16 v[50:65], v[136:139], v[86:89], v[50:65]
	s_mov_b32 m0, s7
	v_mfma_f32_32x32x16_f16 v[66:81], v[140:143], v[82:85], v[66:81]
	v_mfma_f32_32x32x16_f16 v[50:65], v[150:153], v[82:85], v[50:65]
	s_setprio 0
	global_load_lds_dwordx4 v147, s[38:39]
	s_add_u32 s36, s36, 0x2000
	s_addc_u32 s37, s37, 0
	s_add_u32 s38, s38, 0x80
	s_addc_u32 s39, s39, 0
	s_nop 0
